# P0 compress-constant dot product: 64 loads batched instead of 32 serialized load/wait trips
# speedup vs baseline: 1.0036x; 1.0036x over previous
.LBB0_92:
	s_or_b64 exec, exec, s[0:1]
	s_cmpk_gt_i32 s4, 0x7f
	s_cbranch_scc1 .LBB0_98
	s_ashr_i32 s0, s4, 6
	s_ashr_i32 s1, s0, 31
	s_and_b32 s5, s4, 63
	s_lshl_b64 s[2:3], s[0:1], 13
	s_add_u32 s2, s44, s2
	v_mov_b32_e32 v67, 0
	s_addc_u32 s3, s45, s3
	v_lshl_add_u64 v[2:3], s[2:3], 0, v[66:67]
	s_lshl_b64 s[0:1], s[0:1], 19
	s_lshl_b32 s2, s5, 2
	s_add_u32 s2, s46, s2
	s_addc_u32 s3, s47, 0
	s_add_u32 s0, s2, s0
	v_lshlrev_b32_e32 v66, 8, v1
	s_addc_u32 s1, s3, s1
	v_lshl_add_u64 v[4:5], s[0:1], 0, v[66:67]
	v_or_b32_e32 v6, 0xffffffc0, v1
	s_mov_b64 s[0:1], 0
	s_mov_b64 s[2:3], 0x100
	s_mov_b64 s[6:7], 0x4000
	s_movk_i32 s5, 0x7bf
	global_load_dword v130, v[2:3], off
	global_load_dword v162, v[4:5], off
	v_lshl_add_u64 v[2:3], v[2:3], 0, s[2:3]
	v_lshl_add_u64 v[4:5], v[4:5], 0, s[6:7]
	global_load_dword v131, v[2:3], off
	global_load_dword v163, v[4:5], off
	v_lshl_add_u64 v[2:3], v[2:3], 0, s[2:3]
	v_lshl_add_u64 v[4:5], v[4:5], 0, s[6:7]
	global_load_dword v132, v[2:3], off
	global_load_dword v164, v[4:5], off
	v_lshl_add_u64 v[2:3], v[2:3], 0, s[2:3]
	v_lshl_add_u64 v[4:5], v[4:5], 0, s[6:7]
	global_load_dword v133, v[2:3], off
	global_load_dword v165, v[4:5], off
	v_lshl_add_u64 v[2:3], v[2:3], 0, s[2:3]
	v_lshl_add_u64 v[4:5], v[4:5], 0, s[6:7]
	global_load_dword v134, v[2:3], off
	global_load_dword v166, v[4:5], off
	v_lshl_add_u64 v[2:3], v[2:3], 0, s[2:3]
	v_lshl_add_u64 v[4:5], v[4:5], 0, s[6:7]
	global_load_dword v135, v[2:3], off
	global_load_dword v167, v[4:5], off
	v_lshl_add_u64 v[2:3], v[2:3], 0, s[2:3]
	v_lshl_add_u64 v[4:5], v[4:5], 0, s[6:7]
	global_load_dword v136, v[2:3], off
	global_load_dword v168, v[4:5], off
	v_lshl_add_u64 v[2:3], v[2:3], 0, s[2:3]
	v_lshl_add_u64 v[4:5], v[4:5], 0, s[6:7]
	global_load_dword v137, v[2:3], off
	global_load_dword v169, v[4:5], off
	v_lshl_add_u64 v[2:3], v[2:3], 0, s[2:3]
	v_lshl_add_u64 v[4:5], v[4:5], 0, s[6:7]
	global_load_dword v138, v[2:3], off
	global_load_dword v170, v[4:5], off
	v_lshl_add_u64 v[2:3], v[2:3], 0, s[2:3]
	v_lshl_add_u64 v[4:5], v[4:5], 0, s[6:7]
	global_load_dword v139, v[2:3], off
	global_load_dword v171, v[4:5], off
	v_lshl_add_u64 v[2:3], v[2:3], 0, s[2:3]
	v_lshl_add_u64 v[4:5], v[4:5], 0, s[6:7]
	global_load_dword v140, v[2:3], off
	global_load_dword v172, v[4:5], off
	v_lshl_add_u64 v[2:3], v[2:3], 0, s[2:3]
	v_lshl_add_u64 v[4:5], v[4:5], 0, s[6:7]
	global_load_dword v141, v[2:3], off
	global_load_dword v173, v[4:5], off
	v_lshl_add_u64 v[2:3], v[2:3], 0, s[2:3]
	v_lshl_add_u64 v[4:5], v[4:5], 0, s[6:7]
	global_load_dword v142, v[2:3], off
	global_load_dword v174, v[4:5], off
	v_lshl_add_u64 v[2:3], v[2:3], 0, s[2:3]
	v_lshl_add_u64 v[4:5], v[4:5], 0, s[6:7]
	global_load_dword v143, v[2:3], off
	global_load_dword v175, v[4:5], off
	v_lshl_add_u64 v[2:3], v[2:3], 0, s[2:3]
	v_lshl_add_u64 v[4:5], v[4:5], 0, s[6:7]
	global_load_dword v144, v[2:3], off
	global_load_dword v176, v[4:5], off
	v_lshl_add_u64 v[2:3], v[2:3], 0, s[2:3]
	v_lshl_add_u64 v[4:5], v[4:5], 0, s[6:7]
	global_load_dword v145, v[2:3], off
	global_load_dword v177, v[4:5], off
	v_lshl_add_u64 v[2:3], v[2:3], 0, s[2:3]
	v_lshl_add_u64 v[4:5], v[4:5], 0, s[6:7]
	global_load_dword v146, v[2:3], off
	global_load_dword v178, v[4:5], off
	v_lshl_add_u64 v[2:3], v[2:3], 0, s[2:3]
	v_lshl_add_u64 v[4:5], v[4:5], 0, s[6:7]
	global_load_dword v147, v[2:3], off
	global_load_dword v179, v[4:5], off
	v_lshl_add_u64 v[2:3], v[2:3], 0, s[2:3]
	v_lshl_add_u64 v[4:5], v[4:5], 0, s[6:7]
	global_load_dword v148, v[2:3], off
	global_load_dword v180, v[4:5], off
	v_lshl_add_u64 v[2:3], v[2:3], 0, s[2:3]
	v_lshl_add_u64 v[4:5], v[4:5], 0, s[6:7]
	global_load_dword v149, v[2:3], off
	global_load_dword v181, v[4:5], off
	v_lshl_add_u64 v[2:3], v[2:3], 0, s[2:3]
	v_lshl_add_u64 v[4:5], v[4:5], 0, s[6:7]
	global_load_dword v150, v[2:3], off
	global_load_dword v182, v[4:5], off
	v_lshl_add_u64 v[2:3], v[2:3], 0, s[2:3]
	v_lshl_add_u64 v[4:5], v[4:5], 0, s[6:7]
	global_load_dword v151, v[2:3], off
	global_load_dword v183, v[4:5], off
	v_lshl_add_u64 v[2:3], v[2:3], 0, s[2:3]
	v_lshl_add_u64 v[4:5], v[4:5], 0, s[6:7]
	global_load_dword v152, v[2:3], off
	global_load_dword v184, v[4:5], off
	v_lshl_add_u64 v[2:3], v[2:3], 0, s[2:3]
	v_lshl_add_u64 v[4:5], v[4:5], 0, s[6:7]
	global_load_dword v153, v[2:3], off
	global_load_dword v185, v[4:5], off
	v_lshl_add_u64 v[2:3], v[2:3], 0, s[2:3]
	v_lshl_add_u64 v[4:5], v[4:5], 0, s[6:7]
	global_load_dword v154, v[2:3], off
	global_load_dword v186, v[4:5], off
	v_lshl_add_u64 v[2:3], v[2:3], 0, s[2:3]
	v_lshl_add_u64 v[4:5], v[4:5], 0, s[6:7]
	global_load_dword v155, v[2:3], off
	global_load_dword v187, v[4:5], off
	v_lshl_add_u64 v[2:3], v[2:3], 0, s[2:3]
	v_lshl_add_u64 v[4:5], v[4:5], 0, s[6:7]
	global_load_dword v156, v[2:3], off
	global_load_dword v188, v[4:5], off
	v_lshl_add_u64 v[2:3], v[2:3], 0, s[2:3]
	v_lshl_add_u64 v[4:5], v[4:5], 0, s[6:7]
	global_load_dword v157, v[2:3], off
	global_load_dword v189, v[4:5], off
	v_lshl_add_u64 v[2:3], v[2:3], 0, s[2:3]
	v_lshl_add_u64 v[4:5], v[4:5], 0, s[6:7]
	global_load_dword v158, v[2:3], off
	global_load_dword v190, v[4:5], off
	v_lshl_add_u64 v[2:3], v[2:3], 0, s[2:3]
	v_lshl_add_u64 v[4:5], v[4:5], 0, s[6:7]
	global_load_dword v159, v[2:3], off
	global_load_dword v191, v[4:5], off
	v_lshl_add_u64 v[2:3], v[2:3], 0, s[2:3]
	v_lshl_add_u64 v[4:5], v[4:5], 0, s[6:7]
	global_load_dword v160, v[2:3], off
	global_load_dword v192, v[4:5], off
	v_lshl_add_u64 v[2:3], v[2:3], 0, s[2:3]
	v_lshl_add_u64 v[4:5], v[4:5], 0, s[6:7]
	global_load_dword v161, v[2:3], off
	global_load_dword v193, v[4:5], off
	v_lshl_add_u64 v[2:3], v[2:3], 0, s[2:3]
	v_lshl_add_u64 v[4:5], v[4:5], 0, s[6:7]
	s_waitcnt vmcnt(62)
	v_fmac_f32_e32 v67, v130, v162
	s_waitcnt vmcnt(60)
	v_fmac_f32_e32 v67, v131, v163
	s_waitcnt vmcnt(58)
	v_fmac_f32_e32 v67, v132, v164
	s_waitcnt vmcnt(56)
	v_fmac_f32_e32 v67, v133, v165
	s_waitcnt vmcnt(54)
	v_fmac_f32_e32 v67, v134, v166
	s_waitcnt vmcnt(52)
	v_fmac_f32_e32 v67, v135, v167
	s_waitcnt vmcnt(50)
	v_fmac_f32_e32 v67, v136, v168
	s_waitcnt vmcnt(48)
	v_fmac_f32_e32 v67, v137, v169
	s_waitcnt vmcnt(46)
	v_fmac_f32_e32 v67, v138, v170
	s_waitcnt vmcnt(44)
	v_fmac_f32_e32 v67, v139, v171
	s_waitcnt vmcnt(42)
	v_fmac_f32_e32 v67, v140, v172
	s_waitcnt vmcnt(40)
	v_fmac_f32_e32 v67, v141, v173
	s_waitcnt vmcnt(38)
	v_fmac_f32_e32 v67, v142, v174
	s_waitcnt vmcnt(36)
	v_fmac_f32_e32 v67, v143, v175
	s_waitcnt vmcnt(34)
	v_fmac_f32_e32 v67, v144, v176
	s_waitcnt vmcnt(32)
	v_fmac_f32_e32 v67, v145, v177
	s_waitcnt vmcnt(30)
	v_fmac_f32_e32 v67, v146, v178
	s_waitcnt vmcnt(28)
	v_fmac_f32_e32 v67, v147, v179
	s_waitcnt vmcnt(26)
	v_fmac_f32_e32 v67, v148, v180
	s_waitcnt vmcnt(24)
	v_fmac_f32_e32 v67, v149, v181
	s_waitcnt vmcnt(22)
	v_fmac_f32_e32 v67, v150, v182
	s_waitcnt vmcnt(20)
	v_fmac_f32_e32 v67, v151, v183
	s_waitcnt vmcnt(18)
	v_fmac_f32_e32 v67, v152, v184
	s_waitcnt vmcnt(16)
	v_fmac_f32_e32 v67, v153, v185
	s_waitcnt vmcnt(14)
	v_fmac_f32_e32 v67, v154, v186
	s_waitcnt vmcnt(12)
	v_fmac_f32_e32 v67, v155, v187
	s_waitcnt vmcnt(10)
	v_fmac_f32_e32 v67, v156, v188
	s_waitcnt vmcnt(8)
	v_fmac_f32_e32 v67, v157, v189
	s_waitcnt vmcnt(6)
	v_fmac_f32_e32 v67, v158, v190
	s_waitcnt vmcnt(4)
	v_fmac_f32_e32 v67, v159, v191
	s_waitcnt vmcnt(2)
	v_fmac_f32_e32 v67, v160, v192
	s_waitcnt vmcnt(0)
	v_fmac_f32_e32 v67, v161, v193
	s_or_b64 exec, exec, s[0:1]
	v_mbcnt_lo_u32_b32 v2, -1, 0
	v_mbcnt_hi_u32_b32 v3, -1, v2
	v_and_b32_e32 v2, 64, v3
	v_add_u32_e32 v4, 64, v2
	v_xor_b32_e32 v2, 1, v3
	v_cmp_lt_i32_e32 vcc, v2, v4
	v_xor_b32_e32 v5, 2, v3
	v_xor_b32_e32 v6, 4, v3
	v_cndmask_b32_e32 v2, v3, v2, vcc
	v_lshlrev_b32_e32 v2, 2, v2
	ds_bpermute_b32 v2, v2, v67
	v_cmp_lt_i32_e32 vcc, v5, v4
	s_waitcnt lgkmcnt(0)
	v_add_f32_e32 v2, v67, v2
	v_cndmask_b32_e32 v5, v3, v5, vcc
	v_lshlrev_b32_e32 v5, 2, v5
	ds_bpermute_b32 v5, v5, v2
	v_cmp_lt_i32_e32 vcc, v6, v4
	s_waitcnt lgkmcnt(0)
	v_add_f32_e32 v2, v2, v5
	v_cndmask_b32_e32 v5, v3, v6, vcc
	v_lshlrev_b32_e32 v5, 2, v5
	ds_bpermute_b32 v5, v5, v2
	v_xor_b32_e32 v6, 8, v3
	v_cmp_lt_i32_e32 vcc, v6, v4
	s_waitcnt lgkmcnt(0)
	v_add_f32_e32 v2, v2, v5
	v_cndmask_b32_e32 v5, v3, v6, vcc
	v_lshlrev_b32_e32 v5, 2, v5
	ds_bpermute_b32 v5, v5, v2
	v_xor_b32_e32 v6, 16, v3
	v_cmp_lt_i32_e32 vcc, v6, v4
	s_waitcnt lgkmcnt(0)
	v_add_f32_e32 v2, v2, v5
	v_cndmask_b32_e32 v5, v3, v6, vcc
	v_lshlrev_b32_e32 v5, 2, v5
	ds_bpermute_b32 v5, v5, v2
	v_xor_b32_e32 v6, 32, v3
	v_cmp_lt_i32_e32 vcc, v6, v4
	s_waitcnt lgkmcnt(0)
	v_add_f32_e32 v2, v2, v5
	v_cndmask_b32_e32 v3, v3, v6, vcc
	v_lshlrev_b32_e32 v3, 2, v3
	ds_bpermute_b32 v3, v3, v2
	v_cmp_eq_u32_e32 vcc, 0, v1
	s_and_saveexec_b64 s[0:1], vcc
	s_cbranch_execz .LBB0_97
	s_ashr_i32 s5, s4, 31
	s_lshl_b64 s[2:3], s[4:5], 2
	s_add_u32 s2, s92, s2
	s_addc_u32 s3, s93, s3
	s_waitcnt lgkmcnt(0)
	v_add_f32_e32 v1, v2, v3
	v_mov_b32_e32 v2, 0x100000
	global_store_dword v2, v1, s[2:3]
